# v64 + nt hint on the P0 bf16 weight-transpose stores (weights first used in P5/P6/P7)
# speedup vs baseline: 1.0041x; 1.0032x over previous
.LBB0_13:
	s_add_i32 s6, s58, 0xfffff900
	s_cmpk_lt_u32 s6, 0x6000
	s_cbranch_scc1 .LBB0_12
	s_cmpk_gt_i32 s58, 0x4ff
	s_mov_b64 s[2:3], -1
	s_cbranch_scc0 .LBB0_36
	s_cmpk_gt_u32 s58, 0x57f
	s_cbranch_scc0 .LBB0_33
	s_cmpk_gt_u32 s58, 0x5ff
	s_cbranch_scc0 .LBB0_30
	s_cmpk_gt_u32 s58, 0x6ff
	s_cbranch_scc0 .LBB0_27
	s_cmpk_gt_u32 s58, 0x46ff
	s_cbranch_scc0 .LBB0_24
	s_cmpk_gt_u32 s58, 0x66ff
	s_cbranch_scc0 .LBB0_21
	s_add_i32 s0, s58, 0xffff9900
	s_lshr_b32 s0, s0, 5
	s_lshl_b64 s[2:3], s[0:1], 19
	s_lshl_b64 s[60:61], s[0:1], 18
	s_add_u32 s0, s12, s60
	s_addc_u32 s7, s13, s61
	s_and_b32 s33, s16, 0x7c0
	v_or_b32_e32 v4, s33, v105
	v_lshl_add_u64 v[2:3], v[72:73], 0, s[2:3]
	v_lshlrev_b32_e32 v70, 8, v4
	v_lshl_add_u64 v[50:51], v[2:3], 0, v[70:71]
	s_movk_i32 s2, 0x1000
	v_add_co_u32_e32 v30, vcc, s2, v50
	s_movk_i32 s2, 0x2000
	s_nop 0
	v_addc_co_u32_e32 v31, vcc, 0, v51, vcc
	v_add_co_u32_e32 v46, vcc, s2, v50
	s_movk_i32 s2, 0x3000
	s_nop 0
	v_addc_co_u32_e32 v47, vcc, 0, v51, vcc
	v_add_co_u32_e32 v62, vcc, s2, v50
	global_load_dwordx4 v[2:5], v[50:51], off
	global_load_dwordx4 v[6:9], v[50:51], off offset:1024
	global_load_dwordx4 v[10:13], v[50:51], off offset:2048
	global_load_dwordx4 v[14:17], v[50:51], off offset:3072
	v_addc_co_u32_e32 v63, vcc, 0, v51, vcc
	global_load_dwordx4 v[18:21], v[46:47], off offset:-4096
	global_load_dwordx4 v[22:25], v[30:31], off offset:1024
	global_load_dwordx4 v[26:29], v[30:31], off offset:2048
	s_nop 0
	global_load_dwordx4 v[30:33], v[30:31], off offset:3072
	s_nop 0
	global_load_dwordx4 v[34:37], v[46:47], off
	global_load_dwordx4 v[38:41], v[46:47], off offset:1024
	global_load_dwordx4 v[42:45], v[46:47], off offset:2048
	s_nop 0
	global_load_dwordx4 v[46:49], v[46:47], off offset:3072
	s_nop 0
	global_load_dwordx4 v[50:53], v[62:63], off
	global_load_dwordx4 v[54:57], v[62:63], off offset:1024
	global_load_dwordx4 v[58:61], v[62:63], off offset:2048
	s_nop 0
	global_load_dwordx4 v[62:65], v[62:63], off offset:3072
	s_lshl_b32 s2, s33, 1
	s_add_u32 s2, s0, s2
	s_addc_u32 s3, s7, 0
	v_mov_b32_e32 v101, v71
	s_waitcnt vmcnt(14)
	ds_write2_b32 v106, v2, v6 offset1:4
	ds_write2_b32 v106, v3, v7 offset0:65 offset1:69
	ds_write2_b32 v106, v4, v8 offset0:130 offset1:134
	ds_write2_b32 v106, v5, v9 offset0:195 offset1:199
	s_waitcnt vmcnt(12)
	ds_write2_b32 v106, v10, v14 offset0:8 offset1:12
	ds_write2_b32 v106, v11, v15 offset0:73 offset1:77
	ds_write2_b32 v106, v12, v16 offset0:138 offset1:142
	ds_write2_b32 v106, v13, v17 offset0:203 offset1:207
	s_waitcnt vmcnt(10)
	ds_write2_b32 v106, v18, v22 offset0:16 offset1:20
	ds_write2_b32 v106, v19, v23 offset0:81 offset1:85
	ds_write2_b32 v106, v20, v24 offset0:146 offset1:150
	ds_write2_b32 v106, v21, v25 offset0:211 offset1:215
	s_waitcnt vmcnt(8)
	ds_write2_b32 v106, v26, v30 offset0:24 offset1:28
	ds_write2_b32 v106, v27, v31 offset0:89 offset1:93
	ds_write2_b32 v106, v28, v32 offset0:154 offset1:158
	ds_write2_b32 v106, v29, v33 offset0:219 offset1:223
	s_waitcnt vmcnt(6)
	ds_write2_b32 v106, v34, v38 offset0:32 offset1:36
	ds_write2_b32 v106, v35, v39 offset0:97 offset1:101
	ds_write2_b32 v106, v36, v40 offset0:162 offset1:166
	ds_write2_b32 v106, v37, v41 offset0:227 offset1:231
	s_waitcnt vmcnt(4)
	ds_write2_b32 v106, v42, v46 offset0:40 offset1:44
	ds_write2_b32 v106, v43, v47 offset0:105 offset1:109
	ds_write2_b32 v106, v44, v48 offset0:170 offset1:174
	ds_write2_b32 v106, v45, v49 offset0:235 offset1:239
	s_waitcnt vmcnt(2)
	ds_write2_b32 v106, v50, v54 offset0:48 offset1:52
	ds_write2_b32 v106, v51, v55 offset0:113 offset1:117
	ds_write2_b32 v106, v52, v56 offset0:178 offset1:182
	ds_write2_b32 v106, v53, v57 offset0:243 offset1:247
	s_waitcnt vmcnt(0)
	ds_write2_b32 v106, v58, v62 offset0:56 offset1:60
	ds_write2_b32 v106, v59, v63 offset0:121 offset1:125
	ds_write2_b32 v106, v60, v64 offset0:186 offset1:190
	ds_write2_b32 v106, v61, v65 offset0:251 offset1:255
	s_waitcnt lgkmcnt(0)
	ds_read2_b32 v[2:3], v118 offset1:1
	ds_read2_b32 v[4:5], v118 offset0:2 offset1:3
	ds_read2_b32 v[8:9], v118 offset0:6 offset1:7
	v_lshl_add_u64 v[6:7], s[2:3], 0, v[100:101]
	s_mov_b64 s[2:3], 0
	s_waitcnt lgkmcnt(2)
	v_cvt_pk_bf16_f32 v2, v2, v3
	s_waitcnt lgkmcnt(1)
	v_cvt_pk_bf16_f32 v3, v4, v5
	ds_read2_b32 v[4:5], v118 offset0:4 offset1:5
	s_waitcnt lgkmcnt(0)
	v_cvt_pk_bf16_f32 v4, v4, v5
	v_cvt_pk_bf16_f32 v5, v8, v9
	v_lshl_add_u64 v[8:9], v[6:7], 0, v[74:75]
	global_store_dwordx4 v[8:9], v[2:5], off nt
	ds_read2_b32 v[2:3], v119 offset1:1
	ds_read2_b32 v[4:5], v120 offset1:1
	ds_read2_b32 v[8:9], v122 offset1:1
	s_waitcnt lgkmcnt(2)
	v_cvt_pk_bf16_f32 v2, v2, v3
	s_waitcnt lgkmcnt(1)
	v_cvt_pk_bf16_f32 v3, v4, v5
	ds_read2_b32 v[4:5], v121 offset1:1
	s_waitcnt lgkmcnt(0)
	v_cvt_pk_bf16_f32 v4, v4, v5
	v_cvt_pk_bf16_f32 v5, v8, v9
	v_lshl_add_u64 v[8:9], v[6:7], 0, v[76:77]
	global_store_dwordx4 v[8:9], v[2:5], off nt
	ds_read2_b32 v[2:3], v123 offset1:1
	ds_read2_b32 v[4:5], v124 offset1:1
	s_waitcnt lgkmcnt(1)
	v_cvt_pk_bf16_f32 v2, v2, v3
	s_waitcnt lgkmcnt(0)
	v_cvt_pk_bf16_f32 v3, v4, v5
	ds_read2_b32 v[4:5], v125 offset1:1
	s_waitcnt lgkmcnt(0)
	v_cvt_pk_bf16_f32 v4, v4, v5
	v_add_u32_e32 v5, 0x1058, v118
	ds_read2_b32 v[8:9], v5 offset1:1
	s_waitcnt lgkmcnt(0)
	v_cvt_pk_bf16_f32 v5, v8, v9
	v_lshl_add_u64 v[8:9], v[6:7], 0, v[78:79]
	global_store_dwordx4 v[8:9], v[2:5], off nt
	s_nop 1
	v_add_u32_e32 v2, 0x1860, v118
	ds_read2_b32 v[2:3], v2 offset1:1
	s_waitcnt lgkmcnt(0)
	v_cvt_pk_bf16_f32 v2, v2, v3
	v_add_u32_e32 v3, 0x1868, v118
	ds_read2_b32 v[4:5], v3 offset1:1
	s_waitcnt lgkmcnt(0)
	v_cvt_pk_bf16_f32 v3, v4, v5
	v_add_u32_e32 v4, 0x1870, v118
	ds_read2_b32 v[4:5], v4 offset1:1
	s_waitcnt lgkmcnt(0)
	v_cvt_pk_bf16_f32 v4, v4, v5
	v_add_u32_e32 v5, 0x1878, v118
	ds_read2_b32 v[8:9], v5 offset1:1
	s_waitcnt lgkmcnt(0)
	v_cvt_pk_bf16_f32 v5, v8, v9
	v_lshl_add_u64 v[8:9], v[6:7], 0, v[80:81]
	global_store_dwordx4 v[8:9], v[2:5], off nt
	s_nop 1
	v_add_u32_e32 v2, 0x2080, v118
	ds_read2_b32 v[2:3], v2 offset1:1
	s_waitcnt lgkmcnt(0)
	v_cvt_pk_bf16_f32 v2, v2, v3
	v_add_u32_e32 v3, 0x2088, v118
	ds_read2_b32 v[4:5], v3 offset1:1
	s_waitcnt lgkmcnt(0)
	v_cvt_pk_bf16_f32 v3, v4, v5
	v_add_u32_e32 v4, 0x2090, v118
	ds_read2_b32 v[4:5], v4 offset1:1
	s_waitcnt lgkmcnt(0)
	v_cvt_pk_bf16_f32 v4, v4, v5
	v_add_u32_e32 v5, 0x2098, v118
	ds_read2_b32 v[8:9], v5 offset1:1
	s_waitcnt lgkmcnt(0)
	v_cvt_pk_bf16_f32 v5, v8, v9
	v_lshl_add_u64 v[8:9], v[6:7], 0, v[82:83]
	global_store_dwordx4 v[8:9], v[2:5], off nt
	s_nop 1
	v_add_u32_e32 v2, 0x28a0, v118
	ds_read2_b32 v[2:3], v2 offset1:1
	s_waitcnt lgkmcnt(0)
	v_cvt_pk_bf16_f32 v2, v2, v3
	v_add_u32_e32 v3, 0x28a8, v118
	ds_read2_b32 v[4:5], v3 offset1:1
	s_waitcnt lgkmcnt(0)
	v_cvt_pk_bf16_f32 v3, v4, v5
	v_add_u32_e32 v4, 0x28b0, v118
	ds_read2_b32 v[4:5], v4 offset1:1
	s_waitcnt lgkmcnt(0)
	v_cvt_pk_bf16_f32 v4, v4, v5
	v_add_u32_e32 v5, 0x28b8, v118
	ds_read2_b32 v[8:9], v5 offset1:1
	s_waitcnt lgkmcnt(0)
	v_cvt_pk_bf16_f32 v5, v8, v9
	v_lshl_add_u64 v[8:9], v[6:7], 0, v[84:85]
	global_store_dwordx4 v[8:9], v[2:5], off nt
	s_nop 1
	v_add_u32_e32 v2, 0x30c0, v118
	ds_read2_b32 v[2:3], v2 offset1:1
	s_waitcnt lgkmcnt(0)
	v_cvt_pk_bf16_f32 v2, v2, v3
	v_add_u32_e32 v3, 0x30c8, v118
	ds_read2_b32 v[4:5], v3 offset1:1
	s_waitcnt lgkmcnt(0)
	v_cvt_pk_bf16_f32 v3, v4, v5
	v_add_u32_e32 v4, 0x30d0, v118
	ds_read2_b32 v[4:5], v4 offset1:1
	s_waitcnt lgkmcnt(0)
	v_cvt_pk_bf16_f32 v4, v4, v5
	v_add_u32_e32 v5, 0x30d8, v118
	ds_read2_b32 v[8:9], v5 offset1:1
	s_waitcnt lgkmcnt(0)
	v_cvt_pk_bf16_f32 v5, v8, v9
	v_lshl_add_u64 v[8:9], v[6:7], 0, v[86:87]
	global_store_dwordx4 v[8:9], v[2:5], off nt
	v_lshl_add_u64 v[6:7], v[6:7], 0, v[88:89]
	s_nop 0
	v_add_u32_e32 v2, 0x38e0, v118
	ds_read2_b32 v[2:3], v2 offset1:1
	s_waitcnt lgkmcnt(0)
	v_cvt_pk_bf16_f32 v2, v2, v3
	v_add_u32_e32 v3, 0x38e8, v118
	ds_read2_b32 v[4:5], v3 offset1:1
	s_waitcnt lgkmcnt(0)
	v_cvt_pk_bf16_f32 v3, v4, v5
	v_add_u32_e32 v4, 0x38f0, v118
	ds_read2_b32 v[4:5], v4 offset1:1
	s_waitcnt lgkmcnt(0)
	v_cvt_pk_bf16_f32 v4, v4, v5
	v_add_u32_e32 v5, 0x38f8, v118
	ds_read2_b32 v[8:9], v5 offset1:1
	s_waitcnt lgkmcnt(0)
	v_cvt_pk_bf16_f32 v5, v8, v9
	global_store_dwordx4 v[6:7], v[2:5], off nt
	s_waitcnt lgkmcnt(0)

.LBB0_27:
	s_andn2_b64 vcc, exec, s[2:3]
	s_cbranch_vccnz .LBB0_29
	s_and_b32 s0, s18, 0x1fc0
	s_and_b32 s2, s16, 0x3c0
	s_addk_i32 s0, 0xe800
	v_or_b32_e32 v2, s2, v67
	v_readlane_b32 s60, v255, 3
	v_or_b32_e32 v58, s0, v105
	v_lshlrev_b32_e32 v70, 2, v2
	v_readlane_b32 s64, v255, 7
	v_readlane_b32 s65, v255, 8
	v_mov_b32_e32 v59, v71
	v_lshlrev_b64 v[2:3], 12, v[58:59]
	v_lshl_add_u64 v[60:61], s[64:65], 0, v[70:71]
	v_or_b32_e32 v70, 4, v58
	v_lshlrev_b64 v[4:5], 12, v[70:71]
	v_or_b32_e32 v70, 8, v58
	v_lshlrev_b64 v[10:11], 12, v[70:71]
	v_or_b32_e32 v70, 12, v58
	v_lshlrev_b64 v[12:13], 12, v[70:71]
	v_or_b32_e32 v70, 16, v58
	v_lshlrev_b64 v[18:19], 12, v[70:71]
	v_or_b32_e32 v70, 20, v58
	v_lshlrev_b64 v[20:21], 12, v[70:71]
	v_or_b32_e32 v70, 24, v58
	v_lshlrev_b64 v[26:27], 12, v[70:71]
	v_or_b32_e32 v70, 28, v58
	v_lshlrev_b64 v[28:29], 12, v[70:71]
	v_or_b32_e32 v70, 32, v58
	v_lshlrev_b64 v[34:35], 12, v[70:71]
	v_or_b32_e32 v70, 36, v58
	v_lshlrev_b64 v[36:37], 12, v[70:71]
	v_or_b32_e32 v70, 40, v58
	v_lshlrev_b64 v[42:43], 12, v[70:71]
	v_or_b32_e32 v70, 44, v58
	v_lshlrev_b64 v[44:45], 12, v[70:71]
	v_or_b32_e32 v70, 48, v58
	v_lshlrev_b64 v[50:51], 12, v[70:71]
	v_or_b32_e32 v70, 52, v58
	v_lshlrev_b64 v[52:53], 12, v[70:71]
	v_or_b32_e32 v70, 56, v58
	v_lshlrev_b64 v[62:63], 12, v[70:71]
	v_or_b32_e32 v70, 60, v58
	v_lshlrev_b64 v[58:59], 12, v[70:71]
	v_lshl_add_u64 v[2:3], v[60:61], 0, v[2:3]
	v_lshl_add_u64 v[6:7], v[60:61], 0, v[4:5]
	v_lshl_add_u64 v[10:11], v[60:61], 0, v[10:11]
	v_lshl_add_u64 v[14:15], v[60:61], 0, v[12:13]
	v_lshl_add_u64 v[18:19], v[60:61], 0, v[18:19]
	v_lshl_add_u64 v[22:23], v[60:61], 0, v[20:21]
	v_lshl_add_u64 v[26:27], v[60:61], 0, v[26:27]
	v_lshl_add_u64 v[30:31], v[60:61], 0, v[28:29]
	v_lshl_add_u64 v[34:35], v[60:61], 0, v[34:35]
	v_lshl_add_u64 v[38:39], v[60:61], 0, v[36:37]
	v_lshl_add_u64 v[42:43], v[60:61], 0, v[42:43]
	v_lshl_add_u64 v[46:47], v[60:61], 0, v[44:45]
	v_lshl_add_u64 v[50:51], v[60:61], 0, v[50:51]
	v_lshl_add_u64 v[54:55], v[60:61], 0, v[52:53]
	v_lshl_add_u64 v[62:63], v[60:61], 0, v[62:63]
	v_lshl_add_u64 v[64:65], v[60:61], 0, v[58:59]
	global_load_dwordx4 v[2:5], v[2:3], off
	s_nop 0
	global_load_dwordx4 v[6:9], v[6:7], off
	s_nop 0
	global_load_dwordx4 v[10:13], v[10:11], off
	s_nop 0
	global_load_dwordx4 v[14:17], v[14:15], off
	s_nop 0
	global_load_dwordx4 v[18:21], v[18:19], off
	s_nop 0
	global_load_dwordx4 v[22:25], v[22:23], off
	s_nop 0
	global_load_dwordx4 v[26:29], v[26:27], off
	s_nop 0
	global_load_dwordx4 v[30:33], v[30:31], off
	s_nop 0
	global_load_dwordx4 v[34:37], v[34:35], off
	s_nop 0
	global_load_dwordx4 v[38:41], v[38:39], off
	s_nop 0
	global_load_dwordx4 v[42:45], v[42:43], off
	s_nop 0
	global_load_dwordx4 v[46:49], v[46:47], off
	s_nop 0
	global_load_dwordx4 v[50:53], v[50:51], off
	s_nop 0
	global_load_dwordx4 v[54:57], v[54:55], off
	s_nop 0
	global_load_dwordx4 v[58:61], v[62:63], off
	s_nop 0
	global_load_dwordx4 v[62:65], v[64:65], off
	v_readlane_b32 s61, v255, 4
	v_readlane_b32 s62, v255, 5
	v_readlane_b32 s63, v255, 6
	v_readlane_b32 s66, v255, 9
	v_readlane_b32 s67, v255, 10
	v_readlane_b32 s68, v255, 11
	v_readlane_b32 s69, v255, 12
	v_readlane_b32 s70, v255, 13
	v_readlane_b32 s71, v255, 14
	v_readlane_b32 s72, v255, 15
	v_readlane_b32 s73, v255, 16
	v_readlane_b32 s74, v255, 17
	v_readlane_b32 s75, v255, 18
	s_waitcnt vmcnt(14)
	ds_write2_b32 v106, v2, v6 offset1:4
	ds_write2_b32 v106, v3, v7 offset0:65 offset1:69
	ds_write2_b32 v106, v4, v8 offset0:130 offset1:134
	ds_write2_b32 v106, v5, v9 offset0:195 offset1:199
	s_waitcnt vmcnt(12)
	ds_write2_b32 v106, v10, v14 offset0:8 offset1:12
	ds_write2_b32 v106, v11, v15 offset0:73 offset1:77
	ds_write2_b32 v106, v12, v16 offset0:138 offset1:142
	ds_write2_b32 v106, v13, v17 offset0:203 offset1:207
	s_waitcnt vmcnt(10)
	ds_write2_b32 v106, v18, v22 offset0:16 offset1:20
	ds_write2_b32 v106, v19, v23 offset0:81 offset1:85
	ds_write2_b32 v106, v20, v24 offset0:146 offset1:150
	ds_write2_b32 v106, v21, v25 offset0:211 offset1:215
	s_waitcnt vmcnt(8)
	ds_write2_b32 v106, v26, v30 offset0:24 offset1:28
	ds_write2_b32 v106, v27, v31 offset0:89 offset1:93
	ds_write2_b32 v106, v28, v32 offset0:154 offset1:158
	ds_write2_b32 v106, v29, v33 offset0:219 offset1:223
	s_waitcnt vmcnt(6)
	ds_write2_b32 v106, v34, v38 offset0:32 offset1:36
	ds_write2_b32 v106, v35, v39 offset0:97 offset1:101
	ds_write2_b32 v106, v36, v40 offset0:162 offset1:166
	ds_write2_b32 v106, v37, v41 offset0:227 offset1:231
	s_waitcnt vmcnt(4)
	ds_write2_b32 v106, v42, v46 offset0:40 offset1:44
	ds_write2_b32 v106, v43, v47 offset0:105 offset1:109
	ds_write2_b32 v106, v44, v48 offset0:170 offset1:174
	ds_write2_b32 v106, v45, v49 offset0:235 offset1:239
	s_waitcnt vmcnt(2)
	ds_write2_b32 v106, v50, v54 offset0:48 offset1:52
	ds_write2_b32 v106, v51, v55 offset0:113 offset1:117
	ds_write2_b32 v106, v52, v56 offset0:178 offset1:182
	ds_write2_b32 v106, v53, v57 offset0:243 offset1:247
	s_waitcnt vmcnt(0)
	ds_write2_b32 v106, v58, v62 offset0:56 offset1:60
	ds_write2_b32 v106, v59, v63 offset0:121 offset1:125
	ds_write2_b32 v106, v60, v64 offset0:186 offset1:190
	ds_write2_b32 v106, v61, v65 offset0:251 offset1:255
	s_waitcnt lgkmcnt(0)
	ds_read2_b32 v[2:3], v118 offset1:1
	ds_read2_b32 v[4:5], v118 offset0:2 offset1:3
	ds_read2_b32 v[6:7], v118 offset0:4 offset1:5
	ds_read2_b32 v[8:9], v118 offset0:6 offset1:7
	v_lshl_add_u64 v[10:11], s[0:1], 1, v[92:93]
	s_waitcnt lgkmcnt(3)
	v_cvt_pk_bf16_f32 v2, v2, v3
	s_waitcnt lgkmcnt(2)
	v_cvt_pk_bf16_f32 v3, v4, v5
	s_waitcnt lgkmcnt(1)
	v_cvt_pk_bf16_f32 v4, v6, v7
	s_waitcnt lgkmcnt(0)
	v_cvt_pk_bf16_f32 v5, v8, v9
	ds_read2_b32 v[8:9], v119 offset1:1
	ds_read2_b32 v[12:13], v120 offset1:1
	ds_read2_b32 v[14:15], v121 offset1:1
	ds_read2_b32 v[16:17], v122 offset1:1
	v_or_b32_e32 v6, s2, v107
	v_lshlrev_b32_e32 v70, 11, v6
	v_lshl_add_u64 v[6:7], v[10:11], 0, v[70:71]
	global_store_dwordx4 v[6:7], v[2:5], off nt
	v_or_b32_e32 v6, s2, v108
	v_lshlrev_b32_e32 v70, 11, v6
	s_waitcnt lgkmcnt(0)
	v_cvt_pk_bf16_f32 v5, v16, v17
	v_add_u32_e32 v16, 0x1058, v118
	v_cvt_pk_bf16_f32 v2, v8, v9
	v_cvt_pk_bf16_f32 v3, v12, v13
	v_cvt_pk_bf16_f32 v4, v14, v15
	ds_read2_b32 v[8:9], v123 offset1:1
	ds_read2_b32 v[12:13], v124 offset1:1
	ds_read2_b32 v[14:15], v125 offset1:1
	ds_read2_b32 v[16:17], v16 offset1:1
	v_lshl_add_u64 v[6:7], v[10:11], 0, v[70:71]
	global_store_dwordx4 v[6:7], v[2:5], off nt
	v_or_b32_e32 v6, s2, v109
	v_lshlrev_b32_e32 v70, 11, v6
	s_waitcnt lgkmcnt(3)
	v_cvt_pk_bf16_f32 v2, v8, v9
	s_waitcnt lgkmcnt(2)
	v_cvt_pk_bf16_f32 v3, v12, v13
	s_waitcnt lgkmcnt(1)
	v_cvt_pk_bf16_f32 v4, v14, v15
	s_waitcnt lgkmcnt(0)
	v_cvt_pk_bf16_f32 v5, v16, v17
	v_add_u32_e32 v8, 0x1860, v118
	v_add_u32_e32 v12, 0x1868, v118
	v_add_u32_e32 v14, 0x1870, v118
	v_add_u32_e32 v16, 0x1878, v118
	ds_read2_b32 v[8:9], v8 offset1:1
	ds_read2_b32 v[12:13], v12 offset1:1
	ds_read2_b32 v[14:15], v14 offset1:1
	ds_read2_b32 v[16:17], v16 offset1:1
	v_lshl_add_u64 v[6:7], v[10:11], 0, v[70:71]
	global_store_dwordx4 v[6:7], v[2:5], off nt
	v_or_b32_e32 v6, s2, v110
	v_lshlrev_b32_e32 v70, 11, v6
	s_waitcnt lgkmcnt(3)
	v_cvt_pk_bf16_f32 v2, v8, v9
	s_waitcnt lgkmcnt(2)
	v_cvt_pk_bf16_f32 v3, v12, v13
	s_waitcnt lgkmcnt(1)
	v_cvt_pk_bf16_f32 v4, v14, v15
	s_waitcnt lgkmcnt(0)
	v_cvt_pk_bf16_f32 v5, v16, v17
	v_add_u32_e32 v8, 0x2080, v118
	v_add_u32_e32 v12, 0x2088, v118
	v_add_u32_e32 v14, 0x2090, v118
	v_add_u32_e32 v16, 0x2098, v118
	ds_read2_b32 v[8:9], v8 offset1:1
	ds_read2_b32 v[12:13], v12 offset1:1
	ds_read2_b32 v[14:15], v14 offset1:1
	ds_read2_b32 v[16:17], v16 offset1:1
	v_lshl_add_u64 v[6:7], v[10:11], 0, v[70:71]
	global_store_dwordx4 v[6:7], v[2:5], off nt
	v_or_b32_e32 v6, s2, v111
	v_lshlrev_b32_e32 v70, 11, v6
	s_waitcnt lgkmcnt(3)
	v_cvt_pk_bf16_f32 v2, v8, v9
	s_waitcnt lgkmcnt(2)
	v_cvt_pk_bf16_f32 v3, v12, v13
	s_waitcnt lgkmcnt(1)
	v_cvt_pk_bf16_f32 v4, v14, v15
	s_waitcnt lgkmcnt(0)
	v_cvt_pk_bf16_f32 v5, v16, v17
	v_add_u32_e32 v8, 0x28a0, v118
	v_add_u32_e32 v12, 0x28a8, v118
	v_add_u32_e32 v14, 0x28b0, v118
	v_add_u32_e32 v16, 0x28b8, v118
	ds_read2_b32 v[8:9], v8 offset1:1
	ds_read2_b32 v[12:13], v12 offset1:1
	ds_read2_b32 v[14:15], v14 offset1:1
	ds_read2_b32 v[16:17], v16 offset1:1
	v_lshl_add_u64 v[6:7], v[10:11], 0, v[70:71]
	global_store_dwordx4 v[6:7], v[2:5], off nt
	v_or_b32_e32 v6, s2, v112
	v_lshlrev_b32_e32 v70, 11, v6
	s_waitcnt lgkmcnt(3)
	v_cvt_pk_bf16_f32 v2, v8, v9
	s_waitcnt lgkmcnt(2)
	v_cvt_pk_bf16_f32 v3, v12, v13
	s_waitcnt lgkmcnt(1)
	v_cvt_pk_bf16_f32 v4, v14, v15
	s_waitcnt lgkmcnt(0)
	v_cvt_pk_bf16_f32 v5, v16, v17
	v_add_u32_e32 v8, 0x30c0, v118
	v_add_u32_e32 v12, 0x30c8, v118
	v_add_u32_e32 v14, 0x30d0, v118
	v_add_u32_e32 v16, 0x30d8, v118
	ds_read2_b32 v[8:9], v8 offset1:1
	ds_read2_b32 v[12:13], v12 offset1:1
	ds_read2_b32 v[14:15], v14 offset1:1
	ds_read2_b32 v[16:17], v16 offset1:1
	v_lshl_add_u64 v[6:7], v[10:11], 0, v[70:71]
	global_store_dwordx4 v[6:7], v[2:5], off nt
	v_or_b32_e32 v6, s2, v113
	v_lshlrev_b32_e32 v70, 11, v6
	s_waitcnt lgkmcnt(3)
	v_cvt_pk_bf16_f32 v2, v8, v9
	s_waitcnt lgkmcnt(2)
	v_cvt_pk_bf16_f32 v3, v12, v13
	s_waitcnt lgkmcnt(1)
	v_cvt_pk_bf16_f32 v4, v14, v15
	s_waitcnt lgkmcnt(0)
	v_cvt_pk_bf16_f32 v5, v16, v17
	v_add_u32_e32 v8, 0x38e0, v118
	v_add_u32_e32 v12, 0x38e8, v118
	v_add_u32_e32 v14, 0x38f0, v118
	v_add_u32_e32 v16, 0x38f8, v118
	ds_read2_b32 v[8:9], v8 offset1:1
	ds_read2_b32 v[12:13], v12 offset1:1
	ds_read2_b32 v[14:15], v14 offset1:1
	ds_read2_b32 v[16:17], v16 offset1:1
	v_lshl_add_u64 v[6:7], v[10:11], 0, v[70:71]
	global_store_dwordx4 v[6:7], v[2:5], off nt
	v_or_b32_e32 v6, s2, v114
	v_lshlrev_b32_e32 v70, 11, v6
	s_waitcnt lgkmcnt(3)
	v_cvt_pk_bf16_f32 v2, v8, v9
	s_waitcnt lgkmcnt(2)
	v_cvt_pk_bf16_f32 v3, v12, v13
	s_waitcnt lgkmcnt(1)
	v_cvt_pk_bf16_f32 v4, v14, v15
	s_waitcnt lgkmcnt(0)
	v_cvt_pk_bf16_f32 v5, v16, v17
	v_lshl_add_u64 v[6:7], v[10:11], 0, v[70:71]
	global_store_dwordx4 v[6:7], v[2:5], off nt
	s_waitcnt lgkmcnt(0)

.LBB0_30:
	s_andn2_b64 vcc, exec, s[2:3]
	s_cbranch_vccnz .LBB0_32
	s_and_b32 s0, s18, 0x1fc0
	s_and_b32 s2, s16, 0x3c0
	s_addk_i32 s0, 0xea00
	v_or_b32_e32 v2, s2, v67
	v_readlane_b32 s60, v255, 3
	v_or_b32_e32 v58, s0, v105
	v_lshlrev_b32_e32 v70, 2, v2
	v_readlane_b32 s62, v255, 5
	v_readlane_b32 s63, v255, 6
	v_mov_b32_e32 v59, v71
	v_lshlrev_b64 v[2:3], 12, v[58:59]
	v_lshl_add_u64 v[60:61], s[62:63], 0, v[70:71]
	v_or_b32_e32 v70, 4, v58
	v_lshlrev_b64 v[4:5], 12, v[70:71]
	v_or_b32_e32 v70, 8, v58
	v_lshlrev_b64 v[10:11], 12, v[70:71]
	v_or_b32_e32 v70, 12, v58
	v_lshlrev_b64 v[12:13], 12, v[70:71]
	v_or_b32_e32 v70, 16, v58
	v_lshlrev_b64 v[18:19], 12, v[70:71]
	v_or_b32_e32 v70, 20, v58
	v_lshlrev_b64 v[20:21], 12, v[70:71]
	v_or_b32_e32 v70, 24, v58
	v_lshlrev_b64 v[26:27], 12, v[70:71]
	v_or_b32_e32 v70, 28, v58
	v_lshlrev_b64 v[28:29], 12, v[70:71]
	v_or_b32_e32 v70, 32, v58
	v_lshlrev_b64 v[34:35], 12, v[70:71]
	v_or_b32_e32 v70, 36, v58
	v_lshlrev_b64 v[36:37], 12, v[70:71]
	v_or_b32_e32 v70, 40, v58
	v_lshlrev_b64 v[42:43], 12, v[70:71]
	v_or_b32_e32 v70, 44, v58
	v_lshlrev_b64 v[44:45], 12, v[70:71]
	v_or_b32_e32 v70, 48, v58
	v_lshlrev_b64 v[50:51], 12, v[70:71]
	v_or_b32_e32 v70, 52, v58
	v_lshlrev_b64 v[52:53], 12, v[70:71]
	v_or_b32_e32 v70, 56, v58
	v_lshlrev_b64 v[62:63], 12, v[70:71]
	v_or_b32_e32 v70, 60, v58
	v_lshlrev_b64 v[58:59], 12, v[70:71]
	v_lshl_add_u64 v[2:3], v[60:61], 0, v[2:3]
	v_lshl_add_u64 v[6:7], v[60:61], 0, v[4:5]
	v_lshl_add_u64 v[10:11], v[60:61], 0, v[10:11]
	v_lshl_add_u64 v[14:15], v[60:61], 0, v[12:13]
	v_lshl_add_u64 v[18:19], v[60:61], 0, v[18:19]
	v_lshl_add_u64 v[22:23], v[60:61], 0, v[20:21]
	v_lshl_add_u64 v[26:27], v[60:61], 0, v[26:27]
	v_lshl_add_u64 v[30:31], v[60:61], 0, v[28:29]
	v_lshl_add_u64 v[34:35], v[60:61], 0, v[34:35]
	v_lshl_add_u64 v[38:39], v[60:61], 0, v[36:37]
	v_lshl_add_u64 v[42:43], v[60:61], 0, v[42:43]
	v_lshl_add_u64 v[46:47], v[60:61], 0, v[44:45]
	v_lshl_add_u64 v[50:51], v[60:61], 0, v[50:51]
	v_lshl_add_u64 v[54:55], v[60:61], 0, v[52:53]
	v_lshl_add_u64 v[62:63], v[60:61], 0, v[62:63]
	v_lshl_add_u64 v[64:65], v[60:61], 0, v[58:59]
	global_load_dwordx4 v[2:5], v[2:3], off
	s_nop 0
	global_load_dwordx4 v[6:9], v[6:7], off
	s_nop 0
	global_load_dwordx4 v[10:13], v[10:11], off
	s_nop 0
	global_load_dwordx4 v[14:17], v[14:15], off
	s_nop 0
	global_load_dwordx4 v[18:21], v[18:19], off
	s_nop 0
	global_load_dwordx4 v[22:25], v[22:23], off
	s_nop 0
	global_load_dwordx4 v[26:29], v[26:27], off
	s_nop 0
	global_load_dwordx4 v[30:33], v[30:31], off
	s_nop 0
	global_load_dwordx4 v[34:37], v[34:35], off
	s_nop 0
	global_load_dwordx4 v[38:41], v[38:39], off
	s_nop 0
	global_load_dwordx4 v[42:45], v[42:43], off
	s_nop 0
	global_load_dwordx4 v[46:49], v[46:47], off
	s_nop 0
	global_load_dwordx4 v[50:53], v[50:51], off
	s_nop 0
	global_load_dwordx4 v[54:57], v[54:55], off
	s_nop 0
	global_load_dwordx4 v[58:61], v[62:63], off
	s_nop 0
	global_load_dwordx4 v[62:65], v[64:65], off
	v_readlane_b32 s61, v255, 4
	v_readlane_b32 s64, v255, 7
	v_readlane_b32 s65, v255, 8
	v_readlane_b32 s66, v255, 9
	v_readlane_b32 s67, v255, 10
	v_readlane_b32 s68, v255, 11
	v_readlane_b32 s69, v255, 12
	v_readlane_b32 s70, v255, 13
	v_readlane_b32 s71, v255, 14
	v_readlane_b32 s72, v255, 15
	v_readlane_b32 s73, v255, 16
	v_readlane_b32 s74, v255, 17
	v_readlane_b32 s75, v255, 18
	s_waitcnt vmcnt(14)
	ds_write2_b32 v106, v2, v6 offset1:4
	ds_write2_b32 v106, v3, v7 offset0:65 offset1:69
	ds_write2_b32 v106, v4, v8 offset0:130 offset1:134
	ds_write2_b32 v106, v5, v9 offset0:195 offset1:199
	s_waitcnt vmcnt(12)
	ds_write2_b32 v106, v10, v14 offset0:8 offset1:12
	ds_write2_b32 v106, v11, v15 offset0:73 offset1:77
	ds_write2_b32 v106, v12, v16 offset0:138 offset1:142
	ds_write2_b32 v106, v13, v17 offset0:203 offset1:207
	s_waitcnt vmcnt(10)
	ds_write2_b32 v106, v18, v22 offset0:16 offset1:20
	ds_write2_b32 v106, v19, v23 offset0:81 offset1:85
	ds_write2_b32 v106, v20, v24 offset0:146 offset1:150
	ds_write2_b32 v106, v21, v25 offset0:211 offset1:215
	s_waitcnt vmcnt(8)
	ds_write2_b32 v106, v26, v30 offset0:24 offset1:28
	ds_write2_b32 v106, v27, v31 offset0:89 offset1:93
	ds_write2_b32 v106, v28, v32 offset0:154 offset1:158
	ds_write2_b32 v106, v29, v33 offset0:219 offset1:223
	s_waitcnt vmcnt(6)
	ds_write2_b32 v106, v34, v38 offset0:32 offset1:36
	ds_write2_b32 v106, v35, v39 offset0:97 offset1:101
	ds_write2_b32 v106, v36, v40 offset0:162 offset1:166
	ds_write2_b32 v106, v37, v41 offset0:227 offset1:231
	s_waitcnt vmcnt(4)
	ds_write2_b32 v106, v42, v46 offset0:40 offset1:44
	ds_write2_b32 v106, v43, v47 offset0:105 offset1:109
	ds_write2_b32 v106, v44, v48 offset0:170 offset1:174
	ds_write2_b32 v106, v45, v49 offset0:235 offset1:239
	s_waitcnt vmcnt(2)
	ds_write2_b32 v106, v50, v54 offset0:48 offset1:52
	ds_write2_b32 v106, v51, v55 offset0:113 offset1:117
	ds_write2_b32 v106, v52, v56 offset0:178 offset1:182
	ds_write2_b32 v106, v53, v57 offset0:243 offset1:247
	s_waitcnt vmcnt(0)
	ds_write2_b32 v106, v58, v62 offset0:56 offset1:60
	ds_write2_b32 v106, v59, v63 offset0:121 offset1:125
	ds_write2_b32 v106, v60, v64 offset0:186 offset1:190
	ds_write2_b32 v106, v61, v65 offset0:251 offset1:255
	s_waitcnt lgkmcnt(0)
	ds_read2_b32 v[2:3], v118 offset1:1
	ds_read2_b32 v[4:5], v118 offset0:2 offset1:3
	ds_read2_b32 v[6:7], v118 offset0:4 offset1:5
	ds_read2_b32 v[8:9], v118 offset0:6 offset1:7
	v_lshl_add_u64 v[10:11], s[0:1], 1, v[94:95]
	s_waitcnt lgkmcnt(3)
	v_cvt_pk_bf16_f32 v2, v2, v3
	s_waitcnt lgkmcnt(2)
	v_cvt_pk_bf16_f32 v3, v4, v5
	s_waitcnt lgkmcnt(1)
	v_cvt_pk_bf16_f32 v4, v6, v7
	s_waitcnt lgkmcnt(0)
	v_cvt_pk_bf16_f32 v5, v8, v9
	ds_read2_b32 v[8:9], v119 offset1:1
	ds_read2_b32 v[12:13], v120 offset1:1
	ds_read2_b32 v[14:15], v121 offset1:1
	ds_read2_b32 v[16:17], v122 offset1:1
	v_or_b32_e32 v6, s2, v107
	v_lshlrev_b32_e32 v70, 11, v6
	v_lshl_add_u64 v[6:7], v[10:11], 0, v[70:71]
	global_store_dwordx4 v[6:7], v[2:5], off nt
	v_or_b32_e32 v6, s2, v108
	v_lshlrev_b32_e32 v70, 11, v6
	s_waitcnt lgkmcnt(0)
	v_cvt_pk_bf16_f32 v5, v16, v17
	v_add_u32_e32 v16, 0x1058, v118
	v_cvt_pk_bf16_f32 v2, v8, v9
	v_cvt_pk_bf16_f32 v3, v12, v13
	v_cvt_pk_bf16_f32 v4, v14, v15
	ds_read2_b32 v[8:9], v123 offset1:1
	ds_read2_b32 v[12:13], v124 offset1:1
	ds_read2_b32 v[14:15], v125 offset1:1
	ds_read2_b32 v[16:17], v16 offset1:1
	v_lshl_add_u64 v[6:7], v[10:11], 0, v[70:71]
	global_store_dwordx4 v[6:7], v[2:5], off nt
	v_or_b32_e32 v6, s2, v109
	v_lshlrev_b32_e32 v70, 11, v6
	s_waitcnt lgkmcnt(3)
	v_cvt_pk_bf16_f32 v2, v8, v9
	s_waitcnt lgkmcnt(2)
	v_cvt_pk_bf16_f32 v3, v12, v13
	s_waitcnt lgkmcnt(1)
	v_cvt_pk_bf16_f32 v4, v14, v15
	s_waitcnt lgkmcnt(0)
	v_cvt_pk_bf16_f32 v5, v16, v17
	v_add_u32_e32 v8, 0x1860, v118
	v_add_u32_e32 v12, 0x1868, v118
	v_add_u32_e32 v14, 0x1870, v118
	v_add_u32_e32 v16, 0x1878, v118
	ds_read2_b32 v[8:9], v8 offset1:1
	ds_read2_b32 v[12:13], v12 offset1:1
	ds_read2_b32 v[14:15], v14 offset1:1
	ds_read2_b32 v[16:17], v16 offset1:1
	v_lshl_add_u64 v[6:7], v[10:11], 0, v[70:71]
	global_store_dwordx4 v[6:7], v[2:5], off nt
	v_or_b32_e32 v6, s2, v110
	v_lshlrev_b32_e32 v70, 11, v6
	s_waitcnt lgkmcnt(3)
	v_cvt_pk_bf16_f32 v2, v8, v9
	s_waitcnt lgkmcnt(2)
	v_cvt_pk_bf16_f32 v3, v12, v13
	s_waitcnt lgkmcnt(1)
	v_cvt_pk_bf16_f32 v4, v14, v15
	s_waitcnt lgkmcnt(0)
	v_cvt_pk_bf16_f32 v5, v16, v17
	v_add_u32_e32 v8, 0x2080, v118
	v_add_u32_e32 v12, 0x2088, v118
	v_add_u32_e32 v14, 0x2090, v118
	v_add_u32_e32 v16, 0x2098, v118
	ds_read2_b32 v[8:9], v8 offset1:1
	ds_read2_b32 v[12:13], v12 offset1:1
	ds_read2_b32 v[14:15], v14 offset1:1
	ds_read2_b32 v[16:17], v16 offset1:1
	v_lshl_add_u64 v[6:7], v[10:11], 0, v[70:71]
	global_store_dwordx4 v[6:7], v[2:5], off nt
	v_or_b32_e32 v6, s2, v111
	v_lshlrev_b32_e32 v70, 11, v6
	s_waitcnt lgkmcnt(3)
	v_cvt_pk_bf16_f32 v2, v8, v9
	s_waitcnt lgkmcnt(2)
	v_cvt_pk_bf16_f32 v3, v12, v13
	s_waitcnt lgkmcnt(1)
	v_cvt_pk_bf16_f32 v4, v14, v15
	s_waitcnt lgkmcnt(0)
	v_cvt_pk_bf16_f32 v5, v16, v17
	v_add_u32_e32 v8, 0x28a0, v118
	v_add_u32_e32 v12, 0x28a8, v118
	v_add_u32_e32 v14, 0x28b0, v118
	v_add_u32_e32 v16, 0x28b8, v118
	ds_read2_b32 v[8:9], v8 offset1:1
	ds_read2_b32 v[12:13], v12 offset1:1
	ds_read2_b32 v[14:15], v14 offset1:1
	ds_read2_b32 v[16:17], v16 offset1:1
	v_lshl_add_u64 v[6:7], v[10:11], 0, v[70:71]
	global_store_dwordx4 v[6:7], v[2:5], off nt
	v_or_b32_e32 v6, s2, v112
	v_lshlrev_b32_e32 v70, 11, v6
	s_waitcnt lgkmcnt(3)
	v_cvt_pk_bf16_f32 v2, v8, v9
	s_waitcnt lgkmcnt(2)
	v_cvt_pk_bf16_f32 v3, v12, v13
	s_waitcnt lgkmcnt(1)
	v_cvt_pk_bf16_f32 v4, v14, v15
	s_waitcnt lgkmcnt(0)
	v_cvt_pk_bf16_f32 v5, v16, v17
	v_add_u32_e32 v8, 0x30c0, v118
	v_add_u32_e32 v12, 0x30c8, v118
	v_add_u32_e32 v14, 0x30d0, v118
	v_add_u32_e32 v16, 0x30d8, v118
	ds_read2_b32 v[8:9], v8 offset1:1
	ds_read2_b32 v[12:13], v12 offset1:1
	ds_read2_b32 v[14:15], v14 offset1:1
	ds_read2_b32 v[16:17], v16 offset1:1
	v_lshl_add_u64 v[6:7], v[10:11], 0, v[70:71]
	global_store_dwordx4 v[6:7], v[2:5], off nt
	v_or_b32_e32 v6, s2, v113
	v_lshlrev_b32_e32 v70, 11, v6
	s_waitcnt lgkmcnt(3)
	v_cvt_pk_bf16_f32 v2, v8, v9
	s_waitcnt lgkmcnt(2)
	v_cvt_pk_bf16_f32 v3, v12, v13
	s_waitcnt lgkmcnt(1)
	v_cvt_pk_bf16_f32 v4, v14, v15
	s_waitcnt lgkmcnt(0)
	v_cvt_pk_bf16_f32 v5, v16, v17
	v_add_u32_e32 v8, 0x38e0, v118
	v_add_u32_e32 v12, 0x38e8, v118
	v_add_u32_e32 v14, 0x38f0, v118
	v_add_u32_e32 v16, 0x38f8, v118
	ds_read2_b32 v[8:9], v8 offset1:1
	ds_read2_b32 v[12:13], v12 offset1:1
	ds_read2_b32 v[14:15], v14 offset1:1
	ds_read2_b32 v[16:17], v16 offset1:1
	v_lshl_add_u64 v[6:7], v[10:11], 0, v[70:71]
	global_store_dwordx4 v[6:7], v[2:5], off nt
	v_or_b32_e32 v6, s2, v114
	v_lshlrev_b32_e32 v70, 11, v6
	s_waitcnt lgkmcnt(3)
	v_cvt_pk_bf16_f32 v2, v8, v9
	s_waitcnt lgkmcnt(2)
	v_cvt_pk_bf16_f32 v3, v12, v13
	s_waitcnt lgkmcnt(1)
	v_cvt_pk_bf16_f32 v4, v14, v15
	s_waitcnt lgkmcnt(0)
	v_cvt_pk_bf16_f32 v5, v16, v17
	v_lshl_add_u64 v[6:7], v[10:11], 0, v[70:71]
	global_store_dwordx4 v[6:7], v[2:5], off nt
	s_waitcnt lgkmcnt(0)

.LBB0_33:
	s_andn2_b64 vcc, exec, s[2:3]
	s_cbranch_vccnz .LBB0_35
	s_and_b32 s0, s18, 0x1fc0
	s_and_b32 s2, s16, 0x3c0
	s_addk_i32 s0, 0xec00
	v_or_b32_e32 v2, s2, v67
	v_readlane_b32 s60, v255, 3
	v_or_b32_e32 v58, s0, v105
	v_lshlrev_b32_e32 v70, 2, v2
	v_readlane_b32 s61, v255, 4
	v_mov_b32_e32 v59, v71
	v_lshlrev_b64 v[2:3], 12, v[58:59]
	v_lshl_add_u64 v[60:61], s[60:61], 0, v[70:71]
	v_or_b32_e32 v70, 4, v58
	v_lshlrev_b64 v[4:5], 12, v[70:71]
	v_or_b32_e32 v70, 8, v58
	v_lshlrev_b64 v[10:11], 12, v[70:71]
	v_or_b32_e32 v70, 12, v58
	v_lshlrev_b64 v[12:13], 12, v[70:71]
	v_or_b32_e32 v70, 16, v58
	v_lshlrev_b64 v[18:19], 12, v[70:71]
	v_or_b32_e32 v70, 20, v58
	v_lshlrev_b64 v[20:21], 12, v[70:71]
	v_or_b32_e32 v70, 24, v58
	v_lshlrev_b64 v[26:27], 12, v[70:71]
	v_or_b32_e32 v70, 28, v58
	v_lshlrev_b64 v[28:29], 12, v[70:71]
	v_or_b32_e32 v70, 32, v58
	v_lshlrev_b64 v[34:35], 12, v[70:71]
	v_or_b32_e32 v70, 36, v58
	v_lshlrev_b64 v[36:37], 12, v[70:71]
	v_or_b32_e32 v70, 40, v58
	v_lshlrev_b64 v[42:43], 12, v[70:71]
	v_or_b32_e32 v70, 44, v58
	v_lshlrev_b64 v[44:45], 12, v[70:71]
	v_or_b32_e32 v70, 48, v58
	v_lshlrev_b64 v[50:51], 12, v[70:71]
	v_or_b32_e32 v70, 52, v58
	v_lshlrev_b64 v[52:53], 12, v[70:71]
	v_or_b32_e32 v70, 56, v58
	v_lshlrev_b64 v[62:63], 12, v[70:71]
	v_or_b32_e32 v70, 60, v58
	v_lshlrev_b64 v[58:59], 12, v[70:71]
	v_lshl_add_u64 v[2:3], v[60:61], 0, v[2:3]
	v_lshl_add_u64 v[6:7], v[60:61], 0, v[4:5]
	v_lshl_add_u64 v[10:11], v[60:61], 0, v[10:11]
	v_lshl_add_u64 v[14:15], v[60:61], 0, v[12:13]
	v_lshl_add_u64 v[18:19], v[60:61], 0, v[18:19]
	v_lshl_add_u64 v[22:23], v[60:61], 0, v[20:21]
	v_lshl_add_u64 v[26:27], v[60:61], 0, v[26:27]
	v_lshl_add_u64 v[30:31], v[60:61], 0, v[28:29]
	v_lshl_add_u64 v[34:35], v[60:61], 0, v[34:35]
	v_lshl_add_u64 v[38:39], v[60:61], 0, v[36:37]
	v_lshl_add_u64 v[42:43], v[60:61], 0, v[42:43]
	v_lshl_add_u64 v[46:47], v[60:61], 0, v[44:45]
	v_lshl_add_u64 v[50:51], v[60:61], 0, v[50:51]
	v_lshl_add_u64 v[54:55], v[60:61], 0, v[52:53]
	v_lshl_add_u64 v[62:63], v[60:61], 0, v[62:63]
	v_lshl_add_u64 v[64:65], v[60:61], 0, v[58:59]
	global_load_dwordx4 v[2:5], v[2:3], off
	s_nop 0
	global_load_dwordx4 v[6:9], v[6:7], off
	s_nop 0
	global_load_dwordx4 v[10:13], v[10:11], off
	s_nop 0
	global_load_dwordx4 v[14:17], v[14:15], off
	s_nop 0
	global_load_dwordx4 v[18:21], v[18:19], off
	s_nop 0
	global_load_dwordx4 v[22:25], v[22:23], off
	s_nop 0
	global_load_dwordx4 v[26:29], v[26:27], off
	s_nop 0
	global_load_dwordx4 v[30:33], v[30:31], off
	s_nop 0
	global_load_dwordx4 v[34:37], v[34:35], off
	s_nop 0
	global_load_dwordx4 v[38:41], v[38:39], off
	s_nop 0
	global_load_dwordx4 v[42:45], v[42:43], off
	s_nop 0
	global_load_dwordx4 v[46:49], v[46:47], off
	s_nop 0
	global_load_dwordx4 v[50:53], v[50:51], off
	s_nop 0
	global_load_dwordx4 v[54:57], v[54:55], off
	s_nop 0
	global_load_dwordx4 v[58:61], v[62:63], off
	s_nop 0
	global_load_dwordx4 v[62:65], v[64:65], off
	v_readlane_b32 s62, v255, 5
	v_readlane_b32 s63, v255, 6
	v_readlane_b32 s64, v255, 7
	v_readlane_b32 s65, v255, 8
	v_readlane_b32 s66, v255, 9
	v_readlane_b32 s67, v255, 10
	v_readlane_b32 s68, v255, 11
	v_readlane_b32 s69, v255, 12
	v_readlane_b32 s70, v255, 13
	v_readlane_b32 s71, v255, 14
	v_readlane_b32 s72, v255, 15
	v_readlane_b32 s73, v255, 16
	v_readlane_b32 s74, v255, 17
	v_readlane_b32 s75, v255, 18
	s_waitcnt vmcnt(14)
	ds_write2_b32 v106, v2, v6 offset1:4
	ds_write2_b32 v106, v3, v7 offset0:65 offset1:69
	ds_write2_b32 v106, v4, v8 offset0:130 offset1:134
	ds_write2_b32 v106, v5, v9 offset0:195 offset1:199
	s_waitcnt vmcnt(12)
	ds_write2_b32 v106, v10, v14 offset0:8 offset1:12
	ds_write2_b32 v106, v11, v15 offset0:73 offset1:77
	ds_write2_b32 v106, v12, v16 offset0:138 offset1:142
	ds_write2_b32 v106, v13, v17 offset0:203 offset1:207
	s_waitcnt vmcnt(10)
	ds_write2_b32 v106, v18, v22 offset0:16 offset1:20
	ds_write2_b32 v106, v19, v23 offset0:81 offset1:85
	ds_write2_b32 v106, v20, v24 offset0:146 offset1:150
	ds_write2_b32 v106, v21, v25 offset0:211 offset1:215
	s_waitcnt vmcnt(8)
	ds_write2_b32 v106, v26, v30 offset0:24 offset1:28
	ds_write2_b32 v106, v27, v31 offset0:89 offset1:93
	ds_write2_b32 v106, v28, v32 offset0:154 offset1:158
	ds_write2_b32 v106, v29, v33 offset0:219 offset1:223
	s_waitcnt vmcnt(6)
	ds_write2_b32 v106, v34, v38 offset0:32 offset1:36
	ds_write2_b32 v106, v35, v39 offset0:97 offset1:101
	ds_write2_b32 v106, v36, v40 offset0:162 offset1:166
	ds_write2_b32 v106, v37, v41 offset0:227 offset1:231
	s_waitcnt vmcnt(4)
	ds_write2_b32 v106, v42, v46 offset0:40 offset1:44
	ds_write2_b32 v106, v43, v47 offset0:105 offset1:109
	ds_write2_b32 v106, v44, v48 offset0:170 offset1:174
	ds_write2_b32 v106, v45, v49 offset0:235 offset1:239
	s_waitcnt vmcnt(2)
	ds_write2_b32 v106, v50, v54 offset0:48 offset1:52
	ds_write2_b32 v106, v51, v55 offset0:113 offset1:117
	ds_write2_b32 v106, v52, v56 offset0:178 offset1:182
	ds_write2_b32 v106, v53, v57 offset0:243 offset1:247
	s_waitcnt vmcnt(0)
	ds_write2_b32 v106, v58, v62 offset0:56 offset1:60
	ds_write2_b32 v106, v59, v63 offset0:121 offset1:125
	ds_write2_b32 v106, v60, v64 offset0:186 offset1:190
	ds_write2_b32 v106, v61, v65 offset0:251 offset1:255
	s_waitcnt lgkmcnt(0)
	ds_read2_b32 v[2:3], v118 offset1:1
	ds_read2_b32 v[4:5], v118 offset0:2 offset1:3
	ds_read2_b32 v[6:7], v118 offset0:4 offset1:5
	ds_read2_b32 v[8:9], v118 offset0:6 offset1:7
	v_lshl_add_u64 v[10:11], s[0:1], 1, v[96:97]
	s_waitcnt lgkmcnt(3)
	v_cvt_pk_bf16_f32 v2, v2, v3
	s_waitcnt lgkmcnt(2)
	v_cvt_pk_bf16_f32 v3, v4, v5
	s_waitcnt lgkmcnt(1)
	v_cvt_pk_bf16_f32 v4, v6, v7
	s_waitcnt lgkmcnt(0)
	v_cvt_pk_bf16_f32 v5, v8, v9
	ds_read2_b32 v[8:9], v119 offset1:1
	ds_read2_b32 v[12:13], v120 offset1:1
	ds_read2_b32 v[14:15], v121 offset1:1
	ds_read2_b32 v[16:17], v122 offset1:1
	v_or_b32_e32 v6, s2, v107
	v_lshlrev_b32_e32 v70, 11, v6
	v_lshl_add_u64 v[6:7], v[10:11], 0, v[70:71]
	global_store_dwordx4 v[6:7], v[2:5], off nt
	v_or_b32_e32 v6, s2, v108
	v_lshlrev_b32_e32 v70, 11, v6
	s_waitcnt lgkmcnt(0)
	v_cvt_pk_bf16_f32 v5, v16, v17
	v_add_u32_e32 v16, 0x1058, v118
	v_cvt_pk_bf16_f32 v2, v8, v9
	v_cvt_pk_bf16_f32 v3, v12, v13
	v_cvt_pk_bf16_f32 v4, v14, v15
	ds_read2_b32 v[8:9], v123 offset1:1
	ds_read2_b32 v[12:13], v124 offset1:1
	ds_read2_b32 v[14:15], v125 offset1:1
	ds_read2_b32 v[16:17], v16 offset1:1
	v_lshl_add_u64 v[6:7], v[10:11], 0, v[70:71]
	global_store_dwordx4 v[6:7], v[2:5], off nt
	v_or_b32_e32 v6, s2, v109
	v_lshlrev_b32_e32 v70, 11, v6
	s_waitcnt lgkmcnt(3)
	v_cvt_pk_bf16_f32 v2, v8, v9
	s_waitcnt lgkmcnt(2)
	v_cvt_pk_bf16_f32 v3, v12, v13
	s_waitcnt lgkmcnt(1)
	v_cvt_pk_bf16_f32 v4, v14, v15
	s_waitcnt lgkmcnt(0)
	v_cvt_pk_bf16_f32 v5, v16, v17
	v_add_u32_e32 v8, 0x1860, v118
	v_add_u32_e32 v12, 0x1868, v118
	v_add_u32_e32 v14, 0x1870, v118
	v_add_u32_e32 v16, 0x1878, v118
	ds_read2_b32 v[8:9], v8 offset1:1
	ds_read2_b32 v[12:13], v12 offset1:1
	ds_read2_b32 v[14:15], v14 offset1:1
	ds_read2_b32 v[16:17], v16 offset1:1
	v_lshl_add_u64 v[6:7], v[10:11], 0, v[70:71]
	global_store_dwordx4 v[6:7], v[2:5], off nt
	v_or_b32_e32 v6, s2, v110
	v_lshlrev_b32_e32 v70, 11, v6
	s_waitcnt lgkmcnt(3)
	v_cvt_pk_bf16_f32 v2, v8, v9
	s_waitcnt lgkmcnt(2)
	v_cvt_pk_bf16_f32 v3, v12, v13
	s_waitcnt lgkmcnt(1)
	v_cvt_pk_bf16_f32 v4, v14, v15
	s_waitcnt lgkmcnt(0)
	v_cvt_pk_bf16_f32 v5, v16, v17
	v_add_u32_e32 v8, 0x2080, v118
	v_add_u32_e32 v12, 0x2088, v118
	v_add_u32_e32 v14, 0x2090, v118
	v_add_u32_e32 v16, 0x2098, v118
	ds_read2_b32 v[8:9], v8 offset1:1
	ds_read2_b32 v[12:13], v12 offset1:1
	ds_read2_b32 v[14:15], v14 offset1:1
	ds_read2_b32 v[16:17], v16 offset1:1
	v_lshl_add_u64 v[6:7], v[10:11], 0, v[70:71]
	global_store_dwordx4 v[6:7], v[2:5], off nt
	v_or_b32_e32 v6, s2, v111
	v_lshlrev_b32_e32 v70, 11, v6
	s_waitcnt lgkmcnt(3)
	v_cvt_pk_bf16_f32 v2, v8, v9
	s_waitcnt lgkmcnt(2)
	v_cvt_pk_bf16_f32 v3, v12, v13
	s_waitcnt lgkmcnt(1)
	v_cvt_pk_bf16_f32 v4, v14, v15
	s_waitcnt lgkmcnt(0)
	v_cvt_pk_bf16_f32 v5, v16, v17
	v_add_u32_e32 v8, 0x28a0, v118
	v_add_u32_e32 v12, 0x28a8, v118
	v_add_u32_e32 v14, 0x28b0, v118
	v_add_u32_e32 v16, 0x28b8, v118
	ds_read2_b32 v[8:9], v8 offset1:1
	ds_read2_b32 v[12:13], v12 offset1:1
	ds_read2_b32 v[14:15], v14 offset1:1
	ds_read2_b32 v[16:17], v16 offset1:1
	v_lshl_add_u64 v[6:7], v[10:11], 0, v[70:71]
	global_store_dwordx4 v[6:7], v[2:5], off nt
	v_or_b32_e32 v6, s2, v112
	v_lshlrev_b32_e32 v70, 11, v6
	s_waitcnt lgkmcnt(3)
	v_cvt_pk_bf16_f32 v2, v8, v9
	s_waitcnt lgkmcnt(2)
	v_cvt_pk_bf16_f32 v3, v12, v13
	s_waitcnt lgkmcnt(1)
	v_cvt_pk_bf16_f32 v4, v14, v15
	s_waitcnt lgkmcnt(0)
	v_cvt_pk_bf16_f32 v5, v16, v17
	v_add_u32_e32 v8, 0x30c0, v118
	v_add_u32_e32 v12, 0x30c8, v118
	v_add_u32_e32 v14, 0x30d0, v118
	v_add_u32_e32 v16, 0x30d8, v118
	ds_read2_b32 v[8:9], v8 offset1:1
	ds_read2_b32 v[12:13], v12 offset1:1
	ds_read2_b32 v[14:15], v14 offset1:1
	ds_read2_b32 v[16:17], v16 offset1:1
	v_lshl_add_u64 v[6:7], v[10:11], 0, v[70:71]
	global_store_dwordx4 v[6:7], v[2:5], off nt
	v_or_b32_e32 v6, s2, v113
	v_lshlrev_b32_e32 v70, 11, v6
	s_waitcnt lgkmcnt(3)
	v_cvt_pk_bf16_f32 v2, v8, v9
	s_waitcnt lgkmcnt(2)
	v_cvt_pk_bf16_f32 v3, v12, v13
	s_waitcnt lgkmcnt(1)
	v_cvt_pk_bf16_f32 v4, v14, v15
	s_waitcnt lgkmcnt(0)
	v_cvt_pk_bf16_f32 v5, v16, v17
	v_add_u32_e32 v8, 0x38e0, v118
	v_add_u32_e32 v12, 0x38e8, v118
	v_add_u32_e32 v14, 0x38f0, v118
	v_add_u32_e32 v16, 0x38f8, v118
	ds_read2_b32 v[8:9], v8 offset1:1
	ds_read2_b32 v[12:13], v12 offset1:1
	ds_read2_b32 v[14:15], v14 offset1:1
	ds_read2_b32 v[16:17], v16 offset1:1
	v_lshl_add_u64 v[6:7], v[10:11], 0, v[70:71]
	global_store_dwordx4 v[6:7], v[2:5], off nt
	v_or_b32_e32 v6, s2, v114
	v_lshlrev_b32_e32 v70, 11, v6
	s_waitcnt lgkmcnt(3)
	v_cvt_pk_bf16_f32 v2, v8, v9
	s_waitcnt lgkmcnt(2)
	v_cvt_pk_bf16_f32 v3, v12, v13
	s_waitcnt lgkmcnt(1)
	v_cvt_pk_bf16_f32 v4, v14, v15
	s_waitcnt lgkmcnt(0)
	v_cvt_pk_bf16_f32 v5, v16, v17
	v_lshl_add_u64 v[6:7], v[10:11], 0, v[70:71]
	global_store_dwordx4 v[6:7], v[2:5], off nt
	s_waitcnt lgkmcnt(0)
